# rwkv chunk phase cumulative sums: LDS reads issued together instead of one round trip per partial
# baseline (speedup 1.0000x reference)
; template <int CTRL> __device__ __forceinline__ float dpp16(float x) { return __builtin_bit_cast(float, __builtin_amdgcn_update_dpp(0, __builtin_bit_cast(int, x), CTRL, 0xf, 0xf, true)); }
; #define CK_BAR() do { asm volatile("s_waitcnt lgkmcnt(0)" ::: "memory"); __builtin_amdgcn_s_barrier(); asm volatile("" ::: "memory"); } while (0)
; __device__ __forceinline__ void phase1(const int WID_, const In& I, char* lds) {
;     ...
;             for (int e = 0; e < 8; ++e) { const int w_ = e >> 1; const bool hi = e & 1;
;                 auto ex = [&](unsigned u) { return hi ? __builtin_bit_cast(float, u & 0xffff0000u) : __builtin_bit_cast(float, u << 16); };
;                 float x = ex(wr[w_]); r_[e] = x + (ex(pr[w_]) - x) * mur[e];
;                 x = ex(wk[w_]); const float k = x + (ex(pk[w_]) - x) * muk[e];
;                 x = ex(wv4[w_]); v_[e] = x + (ex(pv[w_]) - x) * muv[e];
;                 a_[e] = ex(wa[w_]); kk_[e] = k * ckk[e]; ss += kk_[e] * kk_[e];
;                 kp_[e] = k * (1.f + (a_[e] - 1.f) * cka[e]); rk += r_[e] * kp_[e] * crk[e];
;                 G[s * 64 + cg * 8 + e] = ex(wl[w_]); }
;             ss += dpp16<0xB1>(ss); ss += dpp16<0x4E>(ss); ss += dpp16<0x141>(ss);
;             const float inv = 1.f / fmaxf(sqrtf(ss), 1e-12f);
; #pragma unroll
;             for (int e = 0; e < 8; ++e) { kk_[e] *= inv; b_[e] = kk_[e] * a_[e]; }
;     ...
;         CK_BAR();
;         { const int ch = tid & 63, part = tid >> 6; float run = 0.f;
; #pragma unroll
;           for (int i = 0; i < 8; ++i) { run += G[(8 * part + i) * 64 + ch]; G[(8 * part + i) * 64 + ch] = run; }
;           TOT[part * 64 + ch] = run; }
;         CK_BAR();
;         { const int ch = tid & 63, part = tid >> 6; float off = 0.f;
;           for (int p = 0; p < part; ++p) off += TOT[p * 64 + ch];
; #pragma unroll
;           for (int i = 0; i < 8; ++i) G[(8 * part + i) * 64 + ch] += off; }
.LBB0_1416:
	s_or_b64 exec, exec, s[6:7]
	v_and_b32_e32 v52, 63, v58
	v_ashrrev_i32_e32 v53, 6, v59
	v_lshlrev_b32_e32 v4, 11, v53
	v_lshlrev_b32_e32 v6, 2, v52
	s_waitcnt lgkmcnt(0)
	s_barrier
	v_add3_u32 v4, s77, v4, v6
	ds_read2st64_b32 v[54:55], v4 offset1:1
	ds_read2st64_b32 v[174:175], v4 offset0:2 offset1:3
	ds_read2st64_b32 v[176:177], v4 offset0:4 offset1:5
	ds_read2st64_b32 v[178:179], v4 offset0:6 offset1:7
	v_mov_b32_e32 v5, 0
	v_cmp_lt_i32_e64 s[0:1], 0, v53
	s_waitcnt lgkmcnt(3)
	v_add_f32_e32 v7, 0, v54
	v_add_f32_e32 v63, v7, v55
	ds_write2st64_b32 v4, v7, v63 offset1:1
	s_waitcnt lgkmcnt(3)
	v_add_f32_e32 v7, v63, v174
	v_add_f32_e32 v63, v7, v175
	ds_write2st64_b32 v4, v7, v63 offset0:2 offset1:3
	s_waitcnt lgkmcnt(3)
	v_add_f32_e32 v7, v63, v176
	v_add_f32_e32 v63, v7, v177
	ds_write2st64_b32 v4, v7, v63 offset0:4 offset1:5
	s_waitcnt lgkmcnt(3)
	v_add_f32_e32 v7, v63, v178
	v_add_f32_e32 v54, v7, v179
	ds_write2st64_b32 v4, v7, v54 offset0:6 offset1:7
	v_lshl_add_u32 v7, v59, 2, 0
	v_add_u32_e32 v7, 0x21400, v7
	ds_write_b32 v7, v54
	s_waitcnt lgkmcnt(0)
	s_barrier
	v_readfirstlane_b32 s98, v53
	v_add_u32_e32 v6, 0x21400, v6
	ds_read_b32 v174, v6
	ds_read_b32 v175, v6 offset:256
	ds_read_b32 v176, v6 offset:512
	ds_read_b32 v177, v6 offset:768
	ds_read_b32 v178, v6 offset:1024
	ds_read_b32 v179, v6 offset:1280
	ds_read_b32 v180, v6 offset:1536
	s_cmp_lt_u32 s98, 1
	s_cbranch_scc1 .Lscan_done
	s_waitcnt lgkmcnt(6)
	v_add_f32_e32 v5, v5, v174
	s_cmp_lt_u32 s98, 2
	s_cbranch_scc1 .Lscan_done
	s_waitcnt lgkmcnt(5)
	v_add_f32_e32 v5, v5, v175
	s_cmp_lt_u32 s98, 3
	s_cbranch_scc1 .Lscan_done
	s_waitcnt lgkmcnt(4)
	v_add_f32_e32 v5, v5, v176
	s_cmp_lt_u32 s98, 4
	s_cbranch_scc1 .Lscan_done
	s_waitcnt lgkmcnt(3)
	v_add_f32_e32 v5, v5, v177
	s_cmp_lt_u32 s98, 5
	s_cbranch_scc1 .Lscan_done
	s_waitcnt lgkmcnt(2)
	v_add_f32_e32 v5, v5, v178
	s_cmp_lt_u32 s98, 6
	s_cbranch_scc1 .Lscan_done
	s_waitcnt lgkmcnt(1)
	v_add_f32_e32 v5, v5, v179
	s_cmp_lt_u32 s98, 7
	s_cbranch_scc1 .Lscan_done
	s_waitcnt lgkmcnt(0)
	v_add_f32_e32 v5, v5, v180
.Lscan_done:
	s_waitcnt lgkmcnt(0)
	v_cndmask_b32_e32 v6, 0, v24, vcc
	v_cndmask_b32_e32 v7, 0, v26, vcc
	v_cndmask_b32_e32 v24, 0, v25, vcc
	v_cndmask_b32_e32 v25, 0, v27, vcc
	v_lshlrev_b32_e32 v26, 16, v20
	v_lshlrev_b32_e32 v27, 16, v6
	v_and_b32_e32 v20, 0xffff0000, v20
	v_and_b32_e32 v6, 0xffff0000, v6
	v_sub_f32_e32 v27, v27, v26
	v_sub_f32_e32 v6, v6, v20
	v_fma_mix_f32 v53, v27, v0, v26 op_sel_hi:[0,1,0]
	v_fma_mix_f32 v68, v6, v0, v20 op_sel:[0,1,0] op_sel_hi:[0,1,0]
	v_lshlrev_b32_e32 v0, 16, v21
	v_lshlrev_b32_e32 v6, 16, v24
	v_sub_f32_e32 v6, v6, v0
	v_fma_mix_f32 v72, v6, v1, v0 op_sel_hi:[0,1,0]
	v_and_b32_e32 v0, 0xffff0000, v21
	v_and_b32_e32 v6, 0xffff0000, v24
	v_sub_f32_e32 v6, v6, v0
	v_fma_mix_f32 v73, v6, v1, v0 op_sel:[0,1,0] op_sel_hi:[0,1,0]
	v_lshlrev_b32_e32 v0, 16, v22
	v_lshlrev_b32_e32 v1, 16, v7
	v_sub_f32_e32 v1, v1, v0
	v_fma_mix_f32 v74, v1, v2, v0 op_sel_hi:[0,1,0]
	v_and_b32_e32 v0, 0xffff0000, v22
	v_and_b32_e32 v1, 0xffff0000, v7
	v_sub_f32_e32 v1, v1, v0
	v_fma_mix_f32 v75, v1, v2, v0 op_sel:[0,1,0] op_sel_hi:[0,1,0]
	v_add_f32_e32 v2, v56, v57
	s_mov_b32 s0, 0xf800000
	v_mul_f32_e32 v6, 0x4f800000, v2
	v_cmp_gt_f32_e32 vcc, s0, v2
	v_lshlrev_b32_e32 v0, 16, v23
	v_lshlrev_b32_e32 v1, 16, v25
	v_cndmask_b32_e32 v2, v2, v6, vcc
	v_sqrt_f32_e32 v6, v2
	v_sub_f32_e32 v1, v1, v0
	v_fma_mix_f32 v78, v1, v3, v0 op_sel_hi:[0,1,0]
	v_and_b32_e32 v0, 0xffff0000, v23
	v_add_u32_e32 v1, -1, v6
	v_fma_f32 v7, -v1, v6, v2
	v_cmp_ge_f32_e64 s[0:1], 0, v7
	v_add_u32_e32 v7, 1, v6
	v_lshlrev_b32_e32 v52, 3, v61
	v_cndmask_b32_e64 v1, v6, v1, s[0:1]
	v_fma_f32 v6, -v7, v6, v2
	v_cmp_lt_f32_e64 s[0:1], 0, v6
	s_add_i32 s33, s40, s94
	s_nop 0
	v_cndmask_b32_e64 v1, v1, v7, s[0:1]
	v_mul_f32_e32 v6, 0x37800000, v1
	v_cndmask_b32_e32 v1, v1, v6, vcc
	v_cmp_class_f32_e32 vcc, v2, v77
	v_and_b32_e32 v7, 0xffff0000, v25
	v_sub_f32_e32 v7, v7, v0
	v_cndmask_b32_e32 v1, v1, v2, vcc
	v_max_f32_e32 v1, 0x2b8cbccc, v1
	v_div_scale_f32 v2, s[0:1], v1, v1, 1.0
	v_rcp_f32_e32 v6, v2
	v_fma_mix_f32 v79, v7, v3, v0 op_sel:[0,1,0] op_sel_hi:[0,1,0]
	s_movk_i32 s0, 0xff00
	s_min_i32 s1, s33, 0x1fff
	v_fma_f32 v0, -v2, v6, 1.0
	v_fmac_f32_e32 v6, v0, v6
	v_div_scale_f32 v0, vcc, 1.0, v1, 1.0
	v_mul_f32_e32 v3, v0, v6
	v_fma_f32 v7, -v2, v3, v0
	v_fmac_f32_e32 v3, v7, v6
	v_fma_f32 v0, -v2, v3, v0
	v_div_fmas_f32 v0, v0, v6, v3
	v_div_fixup_f32 v0, v0, v1, 1.0
	v_pk_mul_f32 v[54:55], v[8:9], v[0:1] op_sel_hi:[1,0]
	v_pk_mul_f32 v[50:51], v[50:51], v[0:1] op_sel_hi:[1,0]
	v_pk_mul_f32 v[66:67], v[10:11], v[0:1] op_sel_hi:[1,0]
	v_pk_mul_f32 v[48:49], v[48:49], v[0:1] op_sel_hi:[1,0]
	ds_read2st64_b32 v[0:1], v4 offset1:1
	ds_read2st64_b32 v[2:3], v4 offset0:2 offset1:3
	ds_read2st64_b32 v[6:7], v4 offset0:4 offset1:5
	ds_read2st64_b32 v[8:9], v4 offset0:6 offset1:7
	v_pk_mul_f32 v[56:57], v[54:55], v[44:45]
	v_pk_mul_f32 v[64:65], v[50:51], v[42:43]
	v_cmp_lt_i32_e32 vcc, 0, v60
	s_waitcnt lgkmcnt(3)
	v_add_f32_e32 v0, v5, v0
	v_add_f32_e32 v1, v5, v1
	ds_write2st64_b32 v4, v0, v1 offset1:1
	s_waitcnt lgkmcnt(3)
	v_add_f32_e32 v0, v5, v2
	v_add_f32_e32 v1, v5, v3
	ds_write2st64_b32 v4, v0, v1 offset0:2 offset1:3
	s_waitcnt lgkmcnt(3)
	v_add_f32_e32 v0, v5, v6
	v_add_f32_e32 v1, v5, v7
	ds_write2st64_b32 v4, v0, v1 offset0:4 offset1:5
	s_waitcnt lgkmcnt(3)
	v_add_f32_e32 v0, v5, v8
	v_add_f32_e32 v1, v5, v9
	ds_write2st64_b32 v4, v0, v1 offset0:6 offset1:7
	v_max_i32_e32 v0, 1, v60
	v_lshl_add_u32 v0, v0, 8, s77
	v_lshlrev_b32_e32 v1, 2, v52
	s_waitcnt lgkmcnt(0)
	s_barrier
; __device__ __forceinline__ unsigned pk2(float lo, float hi) { const f32x2h v = {lo, hi}; const bf16x2h b = __builtin_convertvector(v, bf16x2h); return __builtin_bit_cast(unsigned, b); }
; __device__ __forceinline__ bf16 f2bf(float f) { return (bf16)(pk2(f, f) & 0xffffu); }
; __device__ __forceinline__ void phase1(const int WID_, const In& I, char* lds) {
;     ...
;             const float4 g0_ = *(const float4*)(G + s * 64 + cg * 8), g1_ = *(const float4*)(G + s * 64 + cg * 8 + 4);
;             const int sm = (s > 0) ? s - 1 : 0; const float msk = (s > 0) ? 1.f : 0.f;
;             const float4 m0_ = *(const float4*)(G + sm * 64 + cg * 8), m1_ = *(const float4*)(G + sm * 64 + cg * 8 + 4);
;             const float4 l0_ = *(const float4*)(G + 63 * 64 + cg * 8), l1_ = *(const float4*)(G + 63 * 64 + cg * 8 + 4);
;             const float gv_[8] = {g0_.x, g0_.y, g0_.z, g0_.w, g1_.x, g1_.y, g1_.z, g1_.w}, mv_[8] = {m0_.x, m0_.y, m0_.z, m0_.w, m1_.x, m1_.y, m1_.z, m1_.w}, lv_[8] = {l0_.x, l0_.y, l0_.z, l0_.w, l1_.x, l1_.y, l1_.z, l1_.w};
; #pragma unroll
;             for (int e = 0; e < 8; ++e) { const float g = gv_[e], gm1 = mv_[e] * msk, gL = lv_[e];
;                 glast[e] = gL;
;                 const float eg = __expf(g), eng = __expf(-g), egm = __expf(gm1), egl = __expf(gL - g);
;                 ab[e] = -kk_[e] * egm; rb[e] = r_[e] * eg; bb[e] = b_[e] * eng; kb[e] = kp_[e] * eng; bt[e] = b_[e] * egl; kt[e] = kp_[e] * egl; }
; #pragma unroll
;             for (int q = 0; q < 4; ++q) { pab[q] = pk2(ab[2 * q], ab[2 * q + 1]); prb[q] = pk2(rb[2 * q], rb[2 * q + 1]); pbb[q] = pk2(bb[2 * q], bb[2 * q + 1]); pkb[q] = pk2(kb[2 * q], kb[2 * q + 1]); }
;             *(uint4*)(MAT(O_AB) + s * LD + cg * 8) = make_uint4(pab[0], pab[1], pab[2], pab[3]);
;             *(uint4*)(MAT(O_RB) + s * LD + cg * 8) = make_uint4(prb[0], prb[1], prb[2], prb[3]);
;             *(uint4*)(MAT(O_BB) + s * LD + cg * 8) = make_uint4(pbb[0], pbb[1], pbb[2], pbb[3]);
;             *(uint4*)(MAT(O_KB) + s * LD + cg * 8) = make_uint4(pkb[0], pkb[1], pkb[2], pkb[3]);
; #pragma unroll
;             for (int e = 0; e < 8; ++e) { const int k = cg * 8 + e;
;                 MAT(O_AT)[k * LD + s] = f2bf(ab[e]); MAT(O_BT)[k * LD + s] = f2bf(bt[e]); MAT(O_KT)[k * LD + s] = f2bf(kt[e]); MAT(O_VT)[k * LD + s] = f2bf(v_[e]); }
	v_add3_u32 v0, v0, v1, s0
	ds_read_b128 v[8:11], v62
	ds_read_b128 v[20:23], v62 offset:16
	ds_read_b128 v[24:27], v0
	ds_read_b128 v[42:45], v0 offset:16
	v_add_u32_e32 v0, 0, v1
	v_add_u32_e32 v0, 0x21300, v0
	ds_read_b128 v[4:7], v0
	ds_read_b128 v[0:3], v0 offset:16
	v_cndmask_b32_e64 v80, 0, 1.0, vcc
	s_waitcnt lgkmcnt(3)
	v_mul_f32_e32 v63, v80, v24
	v_mul_f32_e32 v24, 0x3fb8aa3b, v8
	v_mul_f32_e32 v62, 0xbfb8aa3b, v8
	s_waitcnt lgkmcnt(1)
	v_sub_f32_e32 v8, v4, v8
	v_mul_f32_e32 v8, 0x3fb8aa3b, v8
	v_exp_f32_e32 v8, v8
	v_mul_f32_e32 v63, 0x3fb8aa3b, v63
	v_exp_f32_e32 v70, v63
	v_mul_f32_e32 v63, 0xbfb8aa3b, v9
	v_mul_f32_e32 v81, v56, v8
	v_mul_f32_e32 v82, v14, v8
	v_mul_f32_e32 v8, v80, v25
	v_mul_f32_e32 v8, 0x3fb8aa3b, v8
	v_exp_f32_e32 v71, v8
	v_sub_f32_e32 v8, v5, v9
	v_mul_f32_e32 v25, 0x3fb8aa3b, v9
	v_mul_f32_e32 v8, 0x3fb8aa3b, v8
	v_exp_f32_e32 v24, v24
	v_exp_f32_e32 v62, v62
	v_exp_f32_e32 v25, v25
	v_exp_f32_e32 v63, v63
	v_exp_f32_e32 v8, v8
	v_mul_f32_e32 v9, v80, v26
	v_pk_mul_f32 v[12:13], v[12:13], v[24:25]
	v_pk_mul_f32 v[24:25], v[56:57], v[62:63]
	v_pk_mul_f32 v[62:63], v[14:15], v[62:63]
	v_mul_f32_e32 v56, v57, v8
	v_mul_f32_e32 v57, v15, v8
	v_mul_f32_e32 v8, 0x3fb8aa3b, v10
	v_mul_f32_e32 v14, 0xbfb8aa3b, v10
	v_sub_f32_e32 v10, v6, v10
	v_mul_f32_e32 v10, 0x3fb8aa3b, v10
	v_exp_f32_e32 v10, v10
	v_pk_mul_f32 v[54:55], v[70:71], v[54:55] neg_lo:[0,1] neg_hi:[0,1]
	v_mul_f32_e32 v9, 0x3fb8aa3b, v9
	v_exp_f32_e32 v26, v9
	v_mul_f32_e32 v70, v64, v10
	v_mul_f32_e32 v71, v28, v10
	v_mul_f32_e32 v10, v80, v27
	v_mul_f32_e32 v9, 0x3fb8aa3b, v11
	v_mul_f32_e32 v15, 0xbfb8aa3b, v11
	v_mul_f32_e32 v10, 0x3fb8aa3b, v10
	v_exp_f32_e32 v8, v8
	v_exp_f32_e32 v14, v14
	v_exp_f32_e32 v9, v9
	v_exp_f32_e32 v15, v15
	v_exp_f32_e32 v27, v10
	v_sub_f32_e32 v10, v7, v11
	v_mul_f32_e32 v10, 0x3fb8aa3b, v10
	v_exp_f32_e32 v83, v10
	v_pk_mul_f32 v[50:51], v[26:27], v[50:51] neg_lo:[0,1] neg_hi:[0,1]
	v_pk_mul_f32 v[10:11], v[36:37], v[8:9]
	v_pk_mul_f32 v[26:27], v[64:65], v[14:15]
	v_pk_mul_f32 v[14:15], v[28:29], v[14:15]
	v_mul_f32_e32 v8, 0x3fb8aa3b, v20
	v_mul_f32_e32 v28, 0xbfb8aa3b, v20
	s_waitcnt lgkmcnt(0)
	v_sub_f32_e32 v20, v0, v20
	v_mul_f32_e32 v20, 0x3fb8aa3b, v20
	v_exp_f32_e32 v20, v20
	v_pk_mul_f32 v[46:47], v[66:67], v[46:47]
	v_mul_f32_e32 v64, v65, v83
	v_mul_f32_e32 v65, v29, v83
	v_mul_f32_e32 v83, v46, v20
	v_mul_f32_e32 v84, v40, v20
	v_mul_f32_e32 v20, v80, v43
	v_mul_f32_e32 v9, v80, v42
	v_mul_f32_e32 v20, 0x3fb8aa3b, v20
	v_mul_f32_e32 v9, 0x3fb8aa3b, v9
	v_exp_f32_e32 v37, v20
	v_sub_f32_e32 v20, v1, v21
	v_exp_f32_e32 v36, v9
	v_mul_f32_e32 v9, 0x3fb8aa3b, v21
	v_mul_f32_e32 v29, 0xbfb8aa3b, v21
	v_mul_f32_e32 v20, 0x3fb8aa3b, v20
	v_sub_f32_e32 v21, v2, v22
	v_exp_f32_e32 v8, v8
	v_exp_f32_e32 v9, v9
	v_exp_f32_e32 v20, v20
	v_mul_f32_e32 v21, 0x3fb8aa3b, v21
	v_exp_f32_e32 v21, v21
	v_exp_f32_e32 v28, v28
	v_exp_f32_e32 v29, v29
	v_pk_mul_f32 v[34:35], v[48:49], v[34:35]
	v_pk_mul_f32 v[36:37], v[36:37], v[66:67] neg_lo:[0,1] neg_hi:[0,1]
	v_pk_mul_f32 v[32:33], v[32:33], v[8:9]
	v_mul_f32_e32 v66, v47, v20
	v_mul_f32_e32 v67, v41, v20
	v_mul_f32_e32 v9, v80, v44
	v_mul_f32_e32 v8, 0x3fb8aa3b, v22
	v_mul_f32_e32 v20, 0xbfb8aa3b, v22
	v_mul_f32_e32 v22, v80, v45
	v_mul_f32_e32 v9, 0x3fb8aa3b, v9
	v_mul_f32_e32 v85, v34, v21
	v_mul_f32_e32 v86, v30, v21
	v_mul_f32_e32 v21, 0xbfb8aa3b, v23
	v_mul_f32_e32 v22, 0x3fb8aa3b, v22
	v_pk_mul_f32 v[42:43], v[46:47], v[28:29]
	v_pk_mul_f32 v[28:29], v[40:41], v[28:29]
	v_exp_f32_e32 v20, v20
	v_exp_f32_e32 v40, v9
	v_mul_f32_e32 v9, 0x3fb8aa3b, v23
	v_exp_f32_e32 v21, v21
	v_exp_f32_e32 v41, v22
	v_sub_f32_e32 v22, v3, v23
	v_exp_f32_e32 v8, v8
	v_exp_f32_e32 v9, v9
	v_mul_f32_e32 v22, 0x3fb8aa3b, v22
	v_exp_f32_e32 v22, v22
	v_pk_mul_f32 v[40:41], v[40:41], v[48:49] neg_lo:[0,1] neg_hi:[0,1]
	v_pk_mul_f32 v[44:45], v[34:35], v[20:21]
	v_pk_mul_f32 v[46:47], v[30:31], v[20:21]
	v_cvt_pk_bf16_f32 v21, v26, v27
	v_cvt_pk_bf16_f32 v26, v28, v29
	v_mul_lo_u32 v28, v60, s9
	v_lshlrev_b32_e32 v29, 1, v52
	v_pk_mul_f32 v[38:39], v[38:39], v[8:9]
	v_cvt_pk_bf16_f32 v8, v54, v55
	v_cvt_pk_bf16_f32 v12, v12, v13
	v_cvt_pk_bf16_f32 v9, v50, v51
	v_cvt_pk_bf16_f32 v13, v10, v11
	v_cvt_pk_bf16_f32 v10, v36, v37
	v_cvt_pk_bf16_f32 v11, v40, v41
	v_add3_u32 v28, 0, v28, v29
	v_mul_f32_e32 v30, v35, v22
	v_mul_f32_e32 v31, v31, v22
	v_cvt_pk_bf16_f32 v20, v24, v25
	v_cvt_pk_bf16_f32 v24, v62, v63
	v_cvt_pk_bf16_f32 v25, v14, v15
	v_cvt_pk_bf16_f32 v14, v32, v33
	v_cvt_pk_bf16_f32 v22, v42, v43
	v_cvt_pk_bf16_f32 v15, v38, v39
	v_cvt_pk_bf16_f32 v23, v44, v45
	v_cvt_pk_bf16_f32 v27, v46, v47
	ds_write_b128 v28, v[8:11]
	ds_write_b128 v28, v[12:15] offset:9216
	ds_write_b128 v28, v[20:23] offset:18432
	ds_write_b128 v28, v[24:27] offset:27648
	v_cvt_pk_bf16_f32 v8, v54, s0
	s_movk_i32 s0, 0x240
	v_mad_u32_u24 v9, v61, s0, v60
	v_lshl_add_u32 v9, v9, 1, 0
	ds_write_b16 v9, v8 offset:36864
	v_cvt_pk_bf16_f32 v8, v81, s0
	ds_write_b16 v9, v8 offset:55296
	v_cvt_pk_bf16_f32 v8, v82, s0
	ds_write_b16 v9, v8 offset:64512
	v_cvt_pk_bf16_f32 v8, v53, s0
	v_add_u32_e32 v10, 0x12000, v9
	ds_write_b16 v10, v8
	v_cvt_pk_bf16_f32 v8, v55, s0
	ds_write_b16 v9, v8 offset:37008
	v_cvt_pk_bf16_f32 v8, v56, s0
	ds_write_b16 v9, v8 offset:55440
	v_cvt_pk_bf16_f32 v8, v57, s0
	ds_write_b16 v9, v8 offset:64656
	v_cvt_pk_bf16_f32 v8, v68, s0
	ds_write_b16 v10, v8 offset:144
	v_cvt_pk_bf16_f32 v8, v50, s0
	ds_write_b16 v9, v8 offset:37152
	v_cvt_pk_bf16_f32 v8, v70, s0
	ds_write_b16 v9, v8 offset:55584
	v_cvt_pk_bf16_f32 v8, v71, s0
	ds_write_b16 v9, v8 offset:64800
	v_cvt_pk_bf16_f32 v8, v72, s0
	ds_write_b16 v10, v8 offset:288
	v_cvt_pk_bf16_f32 v8, v51, s0
	ds_write_b16 v9, v8 offset:37296
	v_cvt_pk_bf16_f32 v8, v64, s0
	ds_write_b16 v9, v8 offset:55728
	v_cvt_pk_bf16_f32 v8, v65, s0
	ds_write_b16 v9, v8 offset:64944
	v_cvt_pk_bf16_f32 v8, v73, s0
	ds_write_b16 v10, v8 offset:432
	v_cvt_pk_bf16_f32 v8, v36, s0
	ds_write_b16 v9, v8 offset:37440
	v_cvt_pk_bf16_f32 v8, v83, s0
	ds_write_b16 v9, v8 offset:55872
	v_cvt_pk_bf16_f32 v8, v84, s0
	ds_write_b16 v9, v8 offset:65088
	v_cvt_pk_bf16_f32 v8, v74, s0
	ds_write_b16 v10, v8 offset:576
	v_cvt_pk_bf16_f32 v8, v37, s0
	ds_write_b16 v9, v8 offset:37584
	v_cvt_pk_bf16_f32 v8, v66, s0
	ds_write_b16 v9, v8 offset:56016
	v_cvt_pk_bf16_f32 v8, v67, s0
	ds_write_b16 v9, v8 offset:65232
	v_cvt_pk_bf16_f32 v8, v75, s0
	ds_write_b16 v10, v8 offset:720
	v_cvt_pk_bf16_f32 v8, v40, s0
	ds_write_b16 v9, v8 offset:37728
	v_cvt_pk_bf16_f32 v8, v85, s0
	ds_write_b16 v9, v8 offset:56160
	v_cvt_pk_bf16_f32 v8, v86, s0
	ds_write_b16 v9, v8 offset:65376
	v_cvt_pk_bf16_f32 v8, v78, s0
	ds_write_b16 v10, v8 offset:864
	v_cvt_pk_bf16_f32 v8, v41, s0
	ds_write_b16 v9, v8 offset:37872
	v_cvt_pk_bf16_f32 v8, v30, s0
	ds_write_b16 v9, v8 offset:56304
	v_cvt_pk_bf16_f32 v8, v31, s0
	ds_write_b16 v9, v8 offset:65520
	v_cvt_pk_bf16_f32 v8, v79, s0
	ds_write_b16 v10, v8 offset:1008
	s_waitcnt lgkmcnt(0)
	s_barrier
; __device__ __forceinline__ void phase1(const int WID_, const In& I, char* lds) {
;     ...
;         P1_LOADS(item + GN);
;         if (s == 63) {
; #pragma unroll
;             for (int e = 0; e < 8; ++e) TOT[cg * 8 + e] = __expf(glast[e]);
;         }
	v_mbcnt_lo_u32_b32 v8, -1, 0
	v_mbcnt_hi_u32_b32 v8, -1, v8
	s_ashr_i32 s0, s1, 10
	v_add_u32_e32 v9, s86, v8
	s_lshr_b32 s4, s1, 1
	s_lshl_b32 s1, s1, 6
	v_ashrrev_i32_e32 v9, 3, v9
	s_and_b32 s4, s4, 0x1c0
	v_lshlrev_b32_e32 v8, 3, v8
	s_and_b32 s1, s1, 0x1fc0
	v_and_or_b32 v14, v8, 56, s4
	v_add_u32_e32 v8, s1, v9
	s_ashr_i32 s1, s0, 31
	s_lshl_b64 s[0:1], s[0:1], 13
	v_ashrrev_i32_e32 v9, 31, v8
	v_lshl_add_u64 v[10:11], s[0:1], 0, v[8:9]
	v_mov_b64_e32 v[12:13], s[92:93]
	v_mad_u64_u32 v[12:13], s[0:1], v10, s8, v[12:13]
	v_mad_i32_i24 v13, v11, s8, v13
	v_lshlrev_b32_e32 v68, 1, v14
	v_cmp_lt_i32_e32 vcc, 0, v8
	v_lshl_add_u64 v[12:13], v[12:13], 0, v[68:69]
	v_readlane_b32 s0, v242, 37
	v_cndmask_b32_e64 v9, 0, -1, vcc
	v_cndmask_b32_e32 v8, 0, v76, vcc
	v_lshl_add_u64 v[8:9], v[12:13], 0, v[8:9]
	global_load_dwordx4 v[36:39], v[12:13], off
	global_load_dwordx4 v[28:31], v[12:13], off offset:1024
	global_load_dwordx4 v[20:23], v[12:13], off offset:2048
	global_load_dwordx4 v[44:47], v[8:9], off
	global_load_dwordx4 v[48:51], v[8:9], off offset:1024
	global_load_dwordx4 v[24:27], v[8:9], off offset:2048
	v_lshlrev_b64 v[8:9], 10, v[10:11]
	v_readlane_b32 s1, v242, 38
	v_cmp_eq_u32_e32 vcc, 63, v60
	s_nop 0
	v_lshl_add_u64 v[10:11], s[0:1], 0, v[8:9]
	v_lshl_add_u64 v[10:11], v[10:11], 0, v[68:69]
	v_lshl_add_u64 v[8:9], s[28:29], 0, v[8:9]
	v_lshl_add_u64 v[8:9], v[8:9], 0, v[68:69]
	global_load_dwordx4 v[32:35], v[10:11], off
	global_load_dwordx4 v[40:43], v[8:9], off
	s_and_saveexec_b64 s[0:1], vcc
	s_cbranch_execz .LBB0_1428
	v_mul_f32_e32 v4, 0x3fb8aa3b, v4
	v_mul_f32_e32 v5, 0x3fb8aa3b, v5
	v_mul_f32_e32 v6, 0x3fb8aa3b, v6
	v_mul_f32_e32 v7, 0x3fb8aa3b, v7
	v_exp_f32_e32 v4, v4
	v_exp_f32_e32 v5, v5
	v_exp_f32_e32 v6, v6
	v_exp_f32_e32 v7, v7
	v_mul_f32_e32 v0, 0x3fb8aa3b, v0
	v_mul_f32_e32 v1, 0x3fb8aa3b, v1
	v_mul_f32_e32 v2, 0x3fb8aa3b, v2
	v_mul_f32_e32 v3, 0x3fb8aa3b, v3
	v_exp_f32_e32 v0, v0
	v_exp_f32_e32 v1, v1
	v_exp_f32_e32 v2, v2
	v_exp_f32_e32 v3, v3
	v_lshl_add_u32 v8, v52, 2, 0
	v_add_u32_e32 v8, 0x21400, v8
	ds_write_b128 v8, v[4:7]
	ds_write_b128 v8, v[0:3] offset:16
